# speedup vs baseline: 1.0061x; 1.0061x over previous
_ZN3att10attn64_fwdEPKDF16_S1_S1_PDF16_S2_P15HIP_vector_typeIfLj2EEPiPKfS2_:
	s_bitcmp1_b32 s2, 8
	s_cbranch_scc0 .Lattn_noprio
	s_setprio 1
.Lattn_noprio:
	s_branch .Lattn_go
	.p2align 8
.Lattn_go:
	s_load_dwordx2 s[4:5], s[0:1], 0x38
	v_lshl_or_b32 v198, s2, 8, v0
	v_ashrrev_i32_e32 v199, 31, v198
	v_lshlrev_b64 v[2:3], 5, v[198:199]
	s_and_b32 s3, s2, 7
	s_waitcnt lgkmcnt(0)
	v_lshl_add_u64 v[2:3], s[4:5], 0, v[2:3]
	global_load_dwordx4 v[134:137], v[2:3], off offset:16 nt
	global_load_dwordx4 v[130:133], v[2:3], off nt
	s_load_dwordx8 s[8:15], s[0:1], 0x0
	s_load_dwordx8 s[16:23], s[0:1], 0x20
	s_lshr_b32 s4, s2, 4
	s_and_b32 s4, s4, 8
	s_or_b32 s33, s4, s3
	s_bfe_u32 s60, s2, 0x30004
	s_and_b32 s4, s2, 8
	s_waitcnt lgkmcnt(0)
	s_lshr_b32 s22, s2, 8
	s_cmp_lg_u32 s60, 7
	s_cselect_b64 s[24:25], -1, 0
	s_cmp_lg_u32 s4, 0
	s_cbranch_scc0 .LBB1_24
	s_and_b64 vcc, exec, s[24:25]
	s_cbranch_vccz .LBB1_25
	s_xor_b32 s62, s60, 15
	v_readfirstlane_b32 s34, v0
	s_mov_b32 s23, 0
	s_lshr_b32 s63, s34, 6
	s_lshl_b64 s[26:27], s[22:23], 11
	s_lshl_b32 s4, s62, 7
	s_lshl_b32 s31, s33, 19
	s_add_u32 s28, s8, s31
	s_addc_u32 s29, s9, 0
	s_or_b32 s4, s26, s4
	s_lshl_b32 s30, s63, 5
	s_add_u32 s6, s4, s30
	s_addc_u32 s7, s27, 0
	s_lshl_b64 s[4:5], s[6:7], 7
	s_add_u32 s28, s28, s4
	s_addc_u32 s29, s29, s5
	s_lshr_b32 s4, s34, 4
	v_and_b32_e32 v200, 7, v0
	s_and_b32 s4, s4, 4
	v_bfe_u32 v224, v0, 4, 2
	v_bitop3_b32 v216, s4, v200, v224 bitop3:0x36
	s_add_u32 s4, s10, s31
	s_addc_u32 s5, s11, 0
	s_lshl_b64 s[38:39], s[22:23], 18
	s_or_b32 s36, s38, 0x24000
	s_add_u32 s4, s4, s36
	s_addc_u32 s5, s5, s39
	s_lshl_b32 s35, s63, 3
	v_bfe_u32 v1, v0, 3, 3
	v_or_b32_e32 v202, s35, v1
	v_mov_b32_e32 v203, 0
	v_lshlrev_b64 v[2:3], 7, v[202:203]
	v_lshl_add_u64 v[2:3], s[4:5], 0, v[2:3]
	s_add_u32 s4, s12, s31
	s_addc_u32 s5, s13, 0
	s_add_u32 s4, s4, s36
	v_lshlrev_b32_e32 v202, 4, v216
	s_addc_u32 s5, s5, s39
	s_lshl_b32 s36, s63, 4
	v_bfe_u32 v223, v0, 2, 4
	v_lshl_add_u64 v[208:209], v[2:3], 0, v[202:203]
	v_or_b32_e32 v202, s36, v223
	s_lshl_b32 s37, s63, 10
	v_lshlrev_b64 v[2:3], 7, v[202:203]
	v_lshlrev_b32_e32 v4, 3, v0
	s_cmp_lg_u32 0, -1
	v_lshl_add_u64 v[2:3], s[4:5], 0, v[2:3]
	v_and_b32_e32 v202, 24, v4
	s_cselect_b32 s4, 0, 0
	v_lshlrev_b32_e32 v4, 1, v202
	v_mov_b32_e32 v5, v203
	s_add_i32 s65, s37, s4
	s_mov_b32 m0, s65
	s_nop 0
	global_load_lds_dwordx4 v[208:209], off
	s_mov_b64 s[4:5], 0x1000
	v_lshl_add_u64 v[210:211], v[2:3], 0, v[4:5]
	v_lshl_add_u64 v[2:3], v[208:209], 0, s[4:5]
	s_add_i32 s40, s65, 0x1000
	s_mov_b32 m0, s40
	s_nop 0
	global_load_lds_dwordx4 v[2:3], off
	s_add_i32 s66, s65, 0x6000
	s_mov_b32 m0, s66
	s_nop 0
	global_load_lds_dwordx4 v[210:211], off
	s_add_i32 s4, s65, 0x7000
	v_lshl_add_u64 v[2:3], v[210:211], 0, 64
	s_mov_b32 m0, s4
	s_nop 0
	global_load_lds_dwordx4 v[2:3], off
	s_mov_b64 s[4:5], 0x2000
	v_lshl_add_u64 v[2:3], v[208:209], 0, s[4:5]
	s_mov_b64 s[42:43], 0x3000
	v_and_b32_e32 v199, 31, v0
	s_add_i32 s31, s65, 0x2000
	s_mov_b32 m0, s31
	s_nop 0
	global_load_lds_dwordx4 v[2:3], off
	v_lshl_add_u64 v[2:3], v[208:209], 0, s[42:43]
	v_bfe_u32 v201, v0, 5, 1
	s_add_i32 s31, s65, 0x3000
	s_mov_b32 m0, s31
	s_nop 0
	global_load_lds_dwordx4 v[2:3], off
	v_lshlrev_b32_e32 v2, 6, v199
	v_lshl_or_b32 v204, v201, 3, v2
	v_lshlrev_b32_e32 v2, 1, v204
	global_load_dwordx4 v[146:149], v2, s[28:29]
	global_load_dwordx4 v[138:141], v2, s[28:29] offset:32
	global_load_dwordx4 v[122:125], v2, s[28:29] offset:64
	global_load_dwordx4 v[114:117], v2, s[28:29] offset:96
	v_lshrrev_b32_e32 v3, 1, v0
	v_bitop3_b32 v3, v201, v3, 7 bitop3:0x78
	s_mov_b64 s[28:29], 0x4000
	v_lshlrev_b32_e32 v219, 4, v3
	v_mov_b32_e32 v2, v203
	v_mov_b32_e32 v3, v203
	v_mov_b32_e32 v4, v203
	v_mov_b32_e32 v6, v203
	v_mov_b32_e32 v7, v203
	v_mov_b32_e32 v8, v203
	v_mov_b32_e32 v9, v203
	v_mov_b32_e32 v10, v203
	v_mov_b32_e32 v11, v203
	v_mov_b32_e32 v12, v203
	v_mov_b32_e32 v13, v203
	v_mov_b32_e32 v14, v203
	v_mov_b32_e32 v15, v203
	v_mov_b32_e32 v16, v203
	v_mov_b32_e32 v17, v203
	v_lshl_add_u64 v[18:19], v[208:209], 0, s[28:29]
	s_add_i32 s28, s65, 0x4000
	v_lshlrev_b32_e32 v227, 7, v199
	s_mov_b32 m0, s28
	s_nop 0
	global_load_lds_dwordx4 v[18:19], off
	s_mov_b64 s[28:29], 0x5000
	v_add_u32_e32 v231, 0, v227
	v_lshl_add_u64 v[18:19], v[208:209], 0, s[28:29]
	s_add_i32 s28, s65, 0x5000
	s_mov_b32 m0, s28
	s_nop 0
	global_load_lds_dwordx4 v[18:19], off
	s_waitcnt vmcnt(6) lgkmcnt(0)
	s_barrier
	v_add_u32_e32 v232, v231, v219
	ds_read_b128 v[34:37], v232
	ds_read_b128 v[38:41], v232 offset:4096
	v_xor_b32_e32 v220, 32, v219
	s_waitcnt vmcnt(3) lgkmcnt(1)
	v_mfma_f32_32x32x16_f16 v[18:33], v[34:37], v[146:149], v[2:17]
	v_add_u32_e32 v233, v231, v220
	v_xor_b32_e32 v221, 64, v219
	v_add_u32_e32 v234, v231, v221
	v_xor_b32_e32 v222, 0x60, v219
	v_add_u32_e32 v235, v231, v222
	s_cmp_lg_u32 s60, 6
	s_cselect_b64 s[28:29], -1, 0
	s_waitcnt lgkmcnt(0)
	v_mfma_f32_32x32x16_f16 v[2:17], v[38:41], v[146:149], v[2:17]
	ds_read_b128 v[34:37], v233
	ds_read_b128 v[38:41], v233 offset:4096
	s_mov_b32 s31, s23
	v_or_b32_e32 v229, s30, v199
	s_and_b64 vcc, exec, s[28:29]
	v_lshlrev_b32_e32 v230, 2, v201
	s_waitcnt vmcnt(2) lgkmcnt(1)
	v_mfma_f32_32x32x16_f16 v[18:33], v[34:37], v[138:141], v[18:33]
	s_waitcnt lgkmcnt(0)
	v_mfma_f32_32x32x16_f16 v[2:17], v[38:41], v[138:141], v[2:17]
	ds_read_b128 v[34:37], v234
	ds_read_b128 v[38:41], v234 offset:4096
	s_waitcnt vmcnt(1) lgkmcnt(1)
	v_mfma_f32_32x32x16_f16 v[18:33], v[34:37], v[122:125], v[18:33]
	s_waitcnt lgkmcnt(0)
	v_mfma_f32_32x32x16_f16 v[2:17], v[38:41], v[122:125], v[2:17]
	ds_read_b128 v[34:37], v235
	ds_read_b128 v[38:41], v235 offset:4096
	s_waitcnt vmcnt(0) lgkmcnt(1)
	v_mfma_f32_32x32x16_f16 v[18:33], v[34:37], v[114:117], v[18:33]
	s_waitcnt lgkmcnt(0)
	v_mfma_f32_32x32x16_f16 v[2:17], v[38:41], v[114:117], v[2:17]
	s_cbranch_vccnz .LBB1_4
	v_or_b32_e32 v34, 32, v230
	v_mov_b32_e32 v35, 0xff800000
	v_cmp_le_u32_e32 vcc, v34, v229
	v_or_b32_e32 v34, 33, v230
	s_nop 6
	v_cndmask_b32_e32 v2, v35, v2, vcc
	v_cmp_lt_u32_e32 vcc, v230, v229
	s_nop 1
	v_cndmask_b32_e32 v19, v35, v19, vcc
	v_cmp_le_u32_e32 vcc, v230, v229
	s_nop 1
	v_cndmask_b32_e32 v18, v35, v18, vcc
	v_cmp_le_u32_e32 vcc, v34, v229
	v_or_b32_e32 v34, 2, v230
	s_nop 0
	v_cndmask_b32_e32 v3, v35, v3, vcc
	v_cmp_le_u32_e32 vcc, v34, v229
	v_or_b32_e32 v34, 34, v230
	s_nop 0
	v_cndmask_b32_e32 v20, v35, v20, vcc
	v_cmp_le_u32_e32 vcc, v34, v229
	v_or_b32_e32 v34, 3, v230
	s_nop 0
	v_cndmask_b32_e32 v4, v35, v4, vcc
	v_cmp_le_u32_e32 vcc, v34, v229
	v_or_b32_e32 v34, 35, v230
	s_nop 0
	v_cndmask_b32_e32 v21, v35, v21, vcc
	v_cmp_le_u32_e32 vcc, v34, v229
	v_or_b32_e32 v34, 8, v230
	s_nop 0
	v_cndmask_b32_e32 v5, v35, v5, vcc
	v_cmp_le_u32_e32 vcc, v34, v229
	v_or_b32_e32 v34, 40, v230
	s_nop 0
	v_cndmask_b32_e32 v22, v35, v22, vcc
	v_cmp_le_u32_e32 vcc, v34, v229
	v_or_b32_e32 v34, 9, v230
	s_nop 0
	v_cndmask_b32_e32 v6, v35, v6, vcc
	v_cmp_le_u32_e32 vcc, v34, v229
	v_or_b32_e32 v34, 41, v230
	s_nop 0
	v_cndmask_b32_e32 v23, v35, v23, vcc
	v_cmp_le_u32_e32 vcc, v34, v229
	v_or_b32_e32 v34, 10, v230
	s_nop 0
	v_cndmask_b32_e32 v7, v35, v7, vcc
	v_cmp_le_u32_e32 vcc, v34, v229
	v_or_b32_e32 v34, 42, v230
	s_nop 0
	v_cndmask_b32_e32 v24, v35, v24, vcc
	v_cmp_le_u32_e32 vcc, v34, v229
	v_or_b32_e32 v34, 11, v230
	s_nop 0
	v_cndmask_b32_e32 v8, v35, v8, vcc
	v_cmp_le_u32_e32 vcc, v34, v229
	v_or_b32_e32 v34, 43, v230
	s_nop 0
	v_cndmask_b32_e32 v25, v35, v25, vcc
	v_cmp_le_u32_e32 vcc, v34, v229
	v_or_b32_e32 v34, 16, v230
	s_nop 0
	v_cndmask_b32_e32 v9, v35, v9, vcc
	v_cmp_le_u32_e32 vcc, v34, v229
	v_or_b32_e32 v34, 48, v230
	s_nop 0
	v_cndmask_b32_e32 v26, v35, v26, vcc
	v_cmp_le_u32_e32 vcc, v34, v229
	v_or_b32_e32 v34, 17, v230
	s_nop 0
	v_cndmask_b32_e32 v10, v35, v10, vcc
	v_cmp_le_u32_e32 vcc, v34, v229
	v_or_b32_e32 v34, 49, v230
	s_nop 0
	v_cndmask_b32_e32 v27, v35, v27, vcc
	v_cmp_le_u32_e32 vcc, v34, v229
	v_or_b32_e32 v34, 18, v230
	s_nop 0
	v_cndmask_b32_e32 v11, v35, v11, vcc
	v_cmp_le_u32_e32 vcc, v34, v229
	v_or_b32_e32 v34, 50, v230
	s_nop 0
	v_cndmask_b32_e32 v28, v35, v28, vcc
	v_cmp_le_u32_e32 vcc, v34, v229
	v_or_b32_e32 v34, 19, v230
	s_nop 0
	v_cndmask_b32_e32 v12, v35, v12, vcc
	v_cmp_le_u32_e32 vcc, v34, v229
	v_or_b32_e32 v34, 51, v230
	s_nop 0
	v_cndmask_b32_e32 v29, v35, v29, vcc
	v_cmp_le_u32_e32 vcc, v34, v229
	v_or_b32_e32 v34, 24, v230
	s_nop 0
	v_cndmask_b32_e32 v13, v35, v13, vcc
	v_cmp_le_u32_e32 vcc, v34, v229
	v_or_b32_e32 v34, 56, v230
	s_nop 0
	v_cndmask_b32_e32 v30, v35, v30, vcc
	v_cmp_le_u32_e32 vcc, v34, v229
	v_or_b32_e32 v34, 25, v230
	s_nop 0
	v_cndmask_b32_e32 v14, v35, v14, vcc
	v_cmp_le_u32_e32 vcc, v34, v229
	v_or_b32_e32 v34, 57, v230
	s_nop 0
	v_cndmask_b32_e32 v31, v35, v31, vcc
	v_cmp_le_u32_e32 vcc, v34, v229
	v_or_b32_e32 v34, 26, v230
	s_nop 0
	v_cndmask_b32_e32 v15, v35, v15, vcc
	v_cmp_le_u32_e32 vcc, v34, v229
	v_or_b32_e32 v34, 58, v230
	s_nop 0
	v_cndmask_b32_e32 v32, v35, v32, vcc
	v_cmp_le_u32_e32 vcc, v34, v229
	v_or_b32_e32 v34, 27, v230
	s_nop 0
	v_cndmask_b32_e32 v16, v35, v16, vcc
	v_cmp_le_u32_e32 vcc, v34, v229
	v_or_b32_e32 v34, 59, v230
	s_nop 0
	v_cndmask_b32_e32 v33, v35, v33, vcc
	v_cmp_le_u32_e32 vcc, v34, v229
	s_nop 1
	v_cndmask_b32_e32 v17, v35, v17, vcc
